# v26 + P11 pair loop: register set R1 refilled straight into free VGPRs v232-247 after its converts; end-of-loop vmcnt(0) and register copies removed
# speedup vs baseline: 1.0030x; 1.0030x over previous
.LBB0_1462:
	s_or_b64 exec, exec, s[2:3]
	s_ashr_i32 s19, s18, 31
	s_lshl_b64 s[2:3], s[16:17], 12
	v_and_b32_e32 v163, 15, v154
	s_add_u32 s44, s24, s2
	s_addc_u32 s45, s25, s3
	v_lshlrev_b32_e32 v0, 8, v163
	v_and_b32_e32 v2, -16, v154
	v_lshl_add_u64 v[8:9], s[44:45], 0, v[0:1]
	v_ashrrev_i32_e32 v3, 31, v2
	v_lshl_add_u64 v[20:21], v[8:9], 0, v[2:3]
	global_load_dwordx4 v[8:11], v[20:21], off nt
	global_load_dwordx4 v[12:15], v[20:21], off offset:64 nt
	global_load_dwordx4 v[16:19], v[20:21], off offset:128 nt
	s_nop 0
	global_load_dwordx4 v[20:23], v[20:21], off offset:192 nt
	s_waitcnt lgkmcnt(0)
	v_or_b32_e32 v0, v6, v4
	v_cmp_ge_i32_e32 vcc, s20, v163
	v_lshl_add_u32 v4, v154, 2, s31
	v_or3_b32 v0, v0, v5, v7
	v_cndmask_b32_e32 v5, 0, v163, vcc
	ds_write_b32 v4, v0
	v_lshl_add_u32 v0, v5, 1, s30
	s_waitcnt lgkmcnt(0)
	ds_read_u16 v0, v0
	v_ashrrev_i32_e32 v164, 4, v154
	s_lshl_b64 s[18:19], s[18:19], 13
	v_lshl_add_u64 v[156:157], s[4:5], 0, v[2:3]
	s_mov_b32 s17, 0
	v_lshl_add_u32 v189, v163, 2, s38
	v_or_b32_e32 v199, 64, v163
	v_mov_b32_e32 v200, 0xff800000
	v_mov_b32_e32 v185, 0
	s_waitcnt vmcnt(3)
	v_cvt_pk_f32_fp8_e32 v[4:5], v8
	v_cvt_pk_f32_fp8_sdwa v[6:7], v8 src0_sel:WORD_1
	v_cvt_pk_f32_fp8_e32 v[24:25], v9
	v_cvt_pk_f32_fp8_sdwa v[8:9], v9 src0_sel:WORD_1
	v_cvt_pk_bf16_f32 v66, v4, v5
	v_or_b32_e32 v4, 16, v163
	v_cmp_ge_i32_e32 vcc, s6, v4
	v_or_b32_e32 v5, 32, v163
	v_cvt_pk_bf16_f32 v67, v6, v7
	v_cndmask_b32_e32 v4, 0, v4, vcc
	v_cmp_ge_i32_e32 vcc, s6, v5
	v_lshl_add_u32 v4, v4, 1, s30
	v_lshlrev_b32_e32 v6, 2, v164
	v_cndmask_b32_e32 v5, 0, v5, vcc
	v_lshl_add_u32 v5, v5, 1, s30
	v_add_u32_e32 v195, s31, v6
	ds_read_u16 v7, v4
	ds_read_u16 v196, v5
	ds_read_b32 v197, v195
	s_waitcnt lgkmcnt(3)
	v_and_b32_e32 v4, 0xffff, v0
	v_mov_b32_e32 v5, s7
	v_lshl_add_u64 v[4:5], s[18:19], 0, v[4:5]
	v_lshlrev_b64 v[4:5], 8, v[4:5]
	v_lshl_add_u64 v[4:5], s[4:5], 0, v[4:5]
	v_lshl_add_u64 v[4:5], v[4:5], 0, v[2:3]
	global_load_dwordx4 v[110:113], v[4:5], off
	global_load_dwordx4 v[106:109], v[4:5], off offset:64
	global_load_dwordx4 v[102:105], v[4:5], off offset:128
	global_load_dwordx4 v[98:101], v[4:5], off offset:192
	s_waitcnt lgkmcnt(2)
	v_and_b32_e32 v4, 0xffff, v7
	v_mov_b32_e32 v5, s7
	v_lshl_add_u64 v[4:5], s[18:19], 0, v[4:5]
	v_lshlrev_b64 v[4:5], 8, v[4:5]
	v_lshl_add_u64 v[4:5], s[4:5], 0, v[4:5]
	v_lshl_add_u64 v[4:5], v[4:5], 0, v[2:3]
	global_load_dwordx4 v[244:247], v[4:5], off
	global_load_dwordx4 v[240:243], v[4:5], off offset:64
	global_load_dwordx4 v[236:239], v[4:5], off offset:128
	global_load_dwordx4 v[232:235], v[4:5], off offset:192
	v_cvt_pk_f32_fp8_e32 v[26:27], v10
	v_cvt_pk_f32_fp8_sdwa v[28:29], v10 src0_sel:WORD_1
	v_cvt_pk_f32_fp8_e32 v[30:31], v11
	v_cvt_pk_f32_fp8_sdwa v[10:11], v11 src0_sel:WORD_1
	s_waitcnt vmcnt(10)
	v_cvt_pk_f32_fp8_e32 v[32:33], v12
	v_cvt_pk_f32_fp8_sdwa v[34:35], v12 src0_sel:WORD_1
	v_cvt_pk_f32_fp8_e32 v[36:37], v13
	v_cvt_pk_f32_fp8_sdwa v[12:13], v13 src0_sel:WORD_1
	v_cvt_pk_f32_fp8_e32 v[38:39], v14
	v_cvt_pk_f32_fp8_sdwa v[40:41], v14 src0_sel:WORD_1
	v_cvt_pk_f32_fp8_e32 v[42:43], v15
	v_cvt_pk_f32_fp8_sdwa v[14:15], v15 src0_sel:WORD_1
	s_waitcnt vmcnt(9)
	v_cvt_pk_f32_fp8_e32 v[44:45], v16
	v_cvt_pk_f32_fp8_sdwa v[46:47], v16 src0_sel:WORD_1
	v_cvt_pk_f32_fp8_e32 v[48:49], v17
	v_cvt_pk_f32_fp8_sdwa v[16:17], v17 src0_sel:WORD_1
	v_lshlrev_b32_e32 v0, 1, v154
	v_bfe_u32 v5, v154, 2, 2
	v_and_b32_e32 v0, 14, v0
	v_bfe_u32 v4, v154, 3, 1
	v_or_b32_e32 v5, v6, v5
	v_lshlrev_b32_e32 v2, 1, v164
	v_cvt_pk_bf16_f32 v69, v8, v9
	v_cvt_pk_bf16_f32 v85, v10, v11
	v_cvt_pk_bf16_f32 v73, v12, v13
	v_cvt_pk_bf16_f32 v89, v14, v15
	v_cvt_pk_bf16_f32 v77, v16, v17
	v_lshlrev_b32_e32 v7, 1, v5
	v_lshlrev_b32_e32 v9, 3, v154
	v_bitop3_b32 v10, v0, v2, v4 bitop3:0x36
	v_or_b32_e32 v11, 1, v2
	v_add_u32_e32 v12, 8, v2
	v_add_u32_e32 v13, 9, v2
	v_add_u32_e32 v14, 16, v2
	v_add_u32_e32 v15, 17, v2
	v_add_u32_e32 v16, 24, v2
	v_add_u32_e32 v2, 25, v2
	v_and_b32_e32 v7, 14, v7
	v_bfe_u32 v8, v164, 1, 1
	v_and_or_b32 v9, v9, 8, s23
	v_bfe_u32 v3, v154, 1, 1
	v_bitop3_b32 v11, v0, v11, v4 bitop3:0x36
	v_bitop3_b32 v12, v0, v12, v4 bitop3:0x36
	v_bitop3_b32 v13, v13, v0, v4 bitop3:0x1e
	v_bitop3_b32 v14, v0, v14, v4 bitop3:0x36
	v_bitop3_b32 v15, v15, v0, v4 bitop3:0x1e
	v_bitop3_b32 v16, v0, v16, v4 bitop3:0x36
	v_bitop3_b32 v0, v2, v0, v4 bitop3:0x1e
	v_lshl_add_u32 v5, v5, 9, v9
	v_lshlrev_b32_e32 v4, 4, v0
	v_bitop3_b32 v0, v7, v3, v8 bitop3:0x36
	v_lshl_add_u32 v177, v0, 4, v5
	v_or_b32_e32 v0, 2, v3
	v_bitop3_b32 v0, v7, v0, v8 bitop3:0x36
	v_lshl_add_u32 v178, v0, 4, v5
	v_or_b32_e32 v0, 4, v3
	v_bitop3_b32 v0, v7, v0, v8 bitop3:0x36
	v_lshl_add_u32 v179, v0, 4, v5
	v_or_b32_e32 v0, 6, v3
	v_bitop3_b32 v0, v7, v0, v8 bitop3:0x36
	v_lshl_add_u32 v180, v0, 4, v5
	v_or_b32_e32 v0, 8, v3
	v_bitop3_b32 v0, v7, v0, v8 bitop3:0x36
	v_lshl_add_u32 v181, v0, 4, v5
	v_or_b32_e32 v0, 10, v3
	v_bitop3_b32 v0, v7, v0, v8 bitop3:0x36
	v_lshl_add_u32 v182, v0, 4, v5
	v_or_b32_e32 v0, 12, v3
	v_bitop3_b32 v0, v7, v0, v8 bitop3:0x36
	v_lshl_add_u32 v183, v0, 4, v5
	v_or_b32_e32 v0, 14, v3
	v_bitop3_b32 v0, v7, v0, v8 bitop3:0x36
	v_lshl_add_u32 v184, v0, 4, v5
	v_or_b32_e32 v0, 16, v3
	v_bitop3_b32 v0, v7, v0, v8 bitop3:0x36
	v_lshl_add_u32 v175, v0, 4, v5
	v_or_b32_e32 v0, 18, v3
	v_bitop3_b32 v0, v7, v0, v8 bitop3:0x36
	v_lshl_add_u32 v176, v0, 4, v5
	v_or_b32_e32 v0, 20, v3
	v_bitop3_b32 v0, v7, v0, v8 bitop3:0x36
	v_lshl_add_u32 v174, v0, 4, v5
	v_or_b32_e32 v0, 22, v3
	v_bitop3_b32 v0, v7, v0, v8 bitop3:0x36
	v_lshl_add_u32 v172, v0, 4, v5
	v_or_b32_e32 v0, 24, v3
	v_bitop3_b32 v0, v7, v0, v8 bitop3:0x36
	v_lshl_add_u32 v173, v0, 4, v5
	v_or_b32_e32 v0, 26, v3
	v_bitop3_b32 v0, v7, v0, v8 bitop3:0x36
	v_lshl_add_u32 v171, v0, 4, v5
	v_or_b32_e32 v0, 28, v3
	v_cvt_pk_f32_fp8_e32 v[50:51], v18
	v_cvt_pk_f32_fp8_sdwa v[52:53], v18 src0_sel:WORD_1
	v_cvt_pk_f32_fp8_e32 v[54:55], v19
	v_cvt_pk_f32_fp8_sdwa v[18:19], v19 src0_sel:WORD_1
	s_waitcnt vmcnt(8)
	v_cvt_pk_f32_fp8_e32 v[56:57], v20
	v_cvt_pk_f32_fp8_sdwa v[58:59], v20 src0_sel:WORD_1
	v_cvt_pk_f32_fp8_e32 v[60:61], v21
	v_cvt_pk_f32_fp8_sdwa v[20:21], v21 src0_sel:WORD_1
	v_cvt_pk_f32_fp8_e32 v[62:63], v22
	v_cvt_pk_f32_fp8_sdwa v[64:65], v22 src0_sel:WORD_1
	v_cvt_pk_f32_fp8_e32 v[96:97], v23
	v_cvt_pk_f32_fp8_sdwa v[22:23], v23 src0_sel:WORD_1
	v_bitop3_b32 v0, v7, v0, v8 bitop3:0x36
	v_lshl_add_u32 v169, v0, 4, v5
	v_or_b32_e32 v0, 30, v3
	v_bitop3_b32 v0, v7, v0, v8 bitop3:0x36
	v_lshl_add_u32 v9, v163, 9, s23
	v_lshlrev_b32_e32 v10, 4, v10
	v_lshlrev_b32_e32 v11, 4, v11
	v_lshlrev_b32_e32 v12, 4, v12
	v_lshlrev_b32_e32 v13, 4, v13
	v_lshlrev_b32_e32 v14, 4, v14
	v_lshlrev_b32_e32 v15, 4, v15
	v_lshlrev_b32_e32 v16, 4, v16
	v_lshl_add_u32 v170, v0, 4, v5
	v_and_or_b32 v0, v6, 60, v159
	v_mov_b32_e32 v2, v1
	v_mov_b32_e32 v3, v1
	v_cvt_pk_bf16_f32 v68, v24, v25
	v_cvt_pk_bf16_f32 v82, v26, v27
	v_cvt_pk_bf16_f32 v83, v28, v29
	v_cvt_pk_bf16_f32 v84, v30, v31
	v_cvt_pk_bf16_f32 v70, v32, v33
	v_cvt_pk_bf16_f32 v71, v34, v35
	v_cvt_pk_bf16_f32 v72, v36, v37
	v_cvt_pk_bf16_f32 v86, v38, v39
	v_cvt_pk_bf16_f32 v87, v40, v41
	v_cvt_pk_bf16_f32 v88, v42, v43
	v_cvt_pk_bf16_f32 v74, v44, v45
	v_cvt_pk_bf16_f32 v75, v46, v47
	v_cvt_pk_bf16_f32 v76, v48, v49
	v_cvt_pk_bf16_f32 v90, v50, v51
	v_cvt_pk_bf16_f32 v91, v52, v53
	v_cvt_pk_bf16_f32 v92, v54, v55
	v_cvt_pk_bf16_f32 v93, v18, v19
	v_cvt_pk_bf16_f32 v78, v56, v57
	v_cvt_pk_bf16_f32 v79, v58, v59
	v_cvt_pk_bf16_f32 v80, v60, v61
	v_cvt_pk_bf16_f32 v81, v20, v21
	v_cvt_pk_bf16_f32 v94, v62, v63
	v_cvt_pk_bf16_f32 v95, v64, v65
	v_cvt_pk_bf16_f32 v96, v96, v97
	v_cvt_pk_bf16_f32 v97, v22, v23
	v_lshlrev_b32_e32 v167, 2, v0
	v_add_u32_e32 v198, s37, v6
	v_mov_b32_e32 v0, v1
	v_add_u32_e32 v193, v9, v10
	v_add_u32_e32 v194, v9, v11
	v_add_u32_e32 v190, v9, v12
	v_add_u32_e32 v191, v9, v13
	v_add_u32_e32 v192, v9, v14
	v_add_u32_e32 v186, v9, v15
	v_add_u32_e32 v187, v9, v16
	v_add_u32_e32 v188, v9, v4
	v_mov_b64_e32 v[64:65], v[2:3]
	v_mov_b64_e32 v[60:61], v[2:3]
	v_mov_b64_e32 v[56:57], v[2:3]
	v_mov_b64_e32 v[52:53], v[2:3]
	v_mov_b64_e32 v[48:49], v[2:3]
	v_mov_b64_e32 v[44:45], v[2:3]
	v_mov_b64_e32 v[40:41], v[2:3]
	v_mov_b64_e32 v[36:37], v[2:3]
	v_mov_b64_e32 v[32:33], v[2:3]
	v_mov_b64_e32 v[28:29], v[2:3]
	v_mov_b64_e32 v[24:25], v[2:3]
	v_mov_b64_e32 v[20:21], v[2:3]
	v_mov_b64_e32 v[16:17], v[2:3]
	v_mov_b64_e32 v[12:13], v[2:3]
	v_mov_b64_e32 v[8:9], v[2:3]
	v_mov_b64_e32 v[62:63], v[0:1]
	v_mov_b64_e32 v[58:59], v[0:1]
	v_mov_b64_e32 v[54:55], v[0:1]
	v_mov_b64_e32 v[50:51], v[0:1]
	v_mov_b64_e32 v[46:47], v[0:1]
	v_mov_b64_e32 v[42:43], v[0:1]
	v_mov_b64_e32 v[38:39], v[0:1]
	v_mov_b64_e32 v[34:35], v[0:1]
	v_mov_b64_e32 v[30:31], v[0:1]
	v_mov_b64_e32 v[26:27], v[0:1]
	v_mov_b64_e32 v[22:23], v[0:1]
	v_mov_b64_e32 v[18:19], v[0:1]
	v_mov_b64_e32 v[14:15], v[0:1]
	v_mov_b64_e32 v[10:11], v[0:1]
	v_mov_b64_e32 v[6:7], v[0:1]
	v_mov_b64_e32 v[4:5], v[2:3]
	v_or_b32_e32 v168, 4, v167
	v_or_b32_e32 v165, 8, v167
	v_or_b32_e32 v166, 12, v167
	v_mov_b64_e32 v[2:3], v[0:1]
.LBB0_1463:
	s_waitcnt lgkmcnt(0)
	v_lshlrev_b32_e32 v0, 6, v197
	v_and_b32_e32 v0, 0x3fc0, v0
	v_add_u32_e32 v0, v189, v0
	v_bfe_u32 v114, v197, 8, 8
	v_bfe_u32 v115, v197, 16, 8
	v_lshrrev_b32_e32 v116, 24, v197
	ds_read_b32 v220, v198
	v_lshl_add_u32 v114, v114, 6, v189
	v_lshl_add_u32 v115, v115, 6, v189
	v_lshl_add_u32 v116, v116, 6, v189
	ds_read_b32 v0, v0
	ds_read_b32 v201, v114
	ds_read_b32 v202, v115
	ds_read_b32 v203, v116
	s_waitcnt vmcnt(7)
	v_cvt_scalef32_pk_bf16_fp8 v114, v110, 1.0
	v_cvt_scalef32_pk_bf16_fp8 v115, v110, 1.0 op_sel:[1,0,0]
	v_cvt_scalef32_pk_bf16_fp8 v116, v111, 1.0
	v_cvt_scalef32_pk_bf16_fp8 v117, v111, 1.0 op_sel:[1,0,0]
	v_cvt_scalef32_pk_bf16_fp8 v118, v112, 1.0
	v_cvt_scalef32_pk_bf16_fp8 v119, v112, 1.0 op_sel:[1,0,0]
	v_cvt_scalef32_pk_bf16_fp8 v120, v113, 1.0
	v_cvt_scalef32_pk_bf16_fp8 v121, v113, 1.0 op_sel:[1,0,0]
	s_waitcnt vmcnt(6)
	v_cvt_scalef32_pk_bf16_fp8 v122, v106, 1.0
	v_cvt_scalef32_pk_bf16_fp8 v123, v106, 1.0 op_sel:[1,0,0]
	v_cvt_scalef32_pk_bf16_fp8 v124, v107, 1.0
	v_cvt_scalef32_pk_bf16_fp8 v125, v107, 1.0 op_sel:[1,0,0]
	v_cvt_scalef32_pk_bf16_fp8 v126, v108, 1.0
	v_cvt_scalef32_pk_bf16_fp8 v127, v108, 1.0 op_sel:[1,0,0]
	v_cvt_scalef32_pk_bf16_fp8 v128, v109, 1.0
	v_cvt_scalef32_pk_bf16_fp8 v129, v109, 1.0 op_sel:[1,0,0]
	s_waitcnt vmcnt(5)
	v_cvt_scalef32_pk_bf16_fp8 v146, v102, 1.0
	v_cvt_scalef32_pk_bf16_fp8 v147, v102, 1.0 op_sel:[1,0,0]
	v_cvt_scalef32_pk_bf16_fp8 v148, v103, 1.0
	v_cvt_scalef32_pk_bf16_fp8 v149, v103, 1.0 op_sel:[1,0,0]
	v_cvt_scalef32_pk_bf16_fp8 v150, v104, 1.0
	v_cvt_scalef32_pk_bf16_fp8 v151, v104, 1.0 op_sel:[1,0,0]
	v_cvt_scalef32_pk_bf16_fp8 v152, v105, 1.0
	v_cvt_scalef32_pk_bf16_fp8 v153, v105, 1.0 op_sel:[1,0,0]
	s_waitcnt vmcnt(4)
	v_cvt_scalef32_pk_bf16_fp8 v204, v98, 1.0
	v_cvt_scalef32_pk_bf16_fp8 v205, v98, 1.0 op_sel:[1,0,0]
	v_cvt_scalef32_pk_bf16_fp8 v206, v99, 1.0
	v_cvt_scalef32_pk_bf16_fp8 v207, v99, 1.0 op_sel:[1,0,0]
	v_cvt_scalef32_pk_bf16_fp8 v208, v100, 1.0
	v_cvt_scalef32_pk_bf16_fp8 v209, v100, 1.0 op_sel:[1,0,0]
	v_cvt_scalef32_pk_bf16_fp8 v210, v101, 1.0
	v_cvt_scalef32_pk_bf16_fp8 v211, v101, 1.0 op_sel:[1,0,0]
	v_and_b32_e32 v98, 0xffff, v196
	v_mov_b32_e32 v99, s7
	v_lshl_add_u64 v[98:99], s[18:19], 0, v[98:99]
	v_lshlrev_b64 v[98:99], 8, v[98:99]
	v_lshl_add_u64 v[98:99], v[156:157], 0, v[98:99]
	global_load_dwordx4 v[110:113], v[98:99], off
	global_load_dwordx4 v[106:109], v[98:99], off offset:64
	global_load_dwordx4 v[102:105], v[98:99], off offset:128
	s_nop 0
	global_load_dwordx4 v[98:101], v[98:99], off offset:192
	v_mfma_f32_16x16x32_bf16 v[212:215], v[114:117], v[66:69], 0
	v_add_u32_e32 v196, -16, v199
	v_cmp_ge_i32_e32 vcc, s6, v196
	v_mfma_f32_16x16x32_bf16 v[212:215], v[122:125], v[70:73], v[212:215]
	s_nop 0
	v_cndmask_b32_e32 v196, 0, v196, vcc
	v_lshl_add_u32 v196, v196, 1, s30
	ds_read_u16 v196, v196
	v_mfma_f32_16x16x32_bf16 v[216:219], v[118:121], v[82:85], 0
	ds_write_b128 v193, v[114:117]
	ds_write_b128 v194, v[118:121]
	ds_write_b128 v190, v[122:125]
	ds_write_b128 v191, v[126:129]
	ds_write_b128 v192, v[146:149]
	ds_write_b128 v186, v[150:153]
	ds_write_b128 v187, v[204:207]
	ds_write_b128 v188, v[208:211]
	v_mfma_f32_16x16x32_bf16 v[114:117], v[146:149], v[74:77], v[212:215]
	ds_read_b32 v197, v198 offset:16
	v_mfma_f32_16x16x32_bf16 v[216:219], v[126:129], v[86:89], v[216:219]
	v_mfma_f32_16x16x32_bf16 v[146:149], v[204:207], v[78:81], v[114:117]
	s_waitcnt lgkmcnt(14)
	s_nop 3
	v_lshlrev_b32_e32 v114, 6, v220
	v_and_b32_e32 v114, 0x3fc0, v114
	v_mfma_f32_16x16x32_bf16 v[118:121], v[150:153], v[90:93], v[216:219]
	v_add_u32_e32 v114, v189, v114
	v_bfe_u32 v115, v220, 8, 8
	v_bfe_u32 v116, v220, 16, 8
	v_lshrrev_b32_e32 v117, 24, v220
	v_lshl_add_u32 v115, v115, 6, v189
	v_lshl_add_u32 v116, v116, 6, v189
	v_lshl_add_u32 v117, v117, 6, v189
	ds_read_b32 v204, v114
	ds_read_b32 v205, v115
	ds_read_b32 v206, v116
	ds_read_b32 v207, v117
	v_mfma_f32_16x16x32_bf16 v[150:153], v[208:211], v[94:97], v[118:121]
	s_waitcnt lgkmcnt(13)
	v_and_b32_e32 v248, 0xffff, v196
	v_mov_b32_e32 v249, s7
	v_lshl_add_u64 v[248:249], s[18:19], 0, v[248:249]
	v_lshlrev_b64 v[248:249], 8, v[248:249]
	v_lshl_add_u64 v[248:249], v[156:157], 0, v[248:249]
	s_cmp_gt_u32 s17, 11
	s_cselect_b64 s[20:21], -1, 0
	s_and_b64 vcc, exec, s[20:21]
	s_cbranch_vccnz .LBB0_1465
	v_cmp_ge_i32_e32 vcc, s6, v199
	s_nop 1
	v_cndmask_b32_e32 v196, 0, v199, vcc
	v_lshl_add_u32 v196, v196, 1, s30
	ds_read_u16 v196, v196
.LBB0_1465:
	v_pk_add_f32 v[148:149], v[148:149], v[152:153]
	v_pk_add_f32 v[146:147], v[146:147], v[150:151]
	v_pk_mul_f32 v[150:151], v[148:149], s[14:15] op_sel_hi:[1,0]
	v_pk_mul_f32 v[146:147], v[146:147], s[14:15] op_sel_hi:[1,0]
	s_waitcnt vmcnt(7)
	v_cvt_scalef32_pk_bf16_fp8 v152, v245, 1.0
	v_add_f32_e32 v149, v0, v146
	v_add_f32_e32 v148, v201, v147
	v_add_f32_e32 v147, v202, v150
	v_add_f32_e32 v146, v203, v151
	v_cvt_scalef32_pk_bf16_fp8 v150, v244, 1.0
	v_cvt_scalef32_pk_bf16_fp8 v151, v244, 1.0 op_sel:[1,0,0]
	v_cvt_scalef32_pk_bf16_fp8 v153, v245, 1.0 op_sel:[1,0,0]
	v_cvt_scalef32_pk_bf16_fp8 v142, v246, 1.0
	v_cvt_scalef32_pk_bf16_fp8 v143, v246, 1.0 op_sel:[1,0,0]
	v_cvt_scalef32_pk_bf16_fp8 v144, v247, 1.0
	v_cvt_scalef32_pk_bf16_fp8 v145, v247, 1.0 op_sel:[1,0,0]
	s_waitcnt vmcnt(6)
	v_cvt_scalef32_pk_bf16_fp8 v208, v240, 1.0
	v_cvt_scalef32_pk_bf16_fp8 v209, v240, 1.0 op_sel:[1,0,0]
	v_cvt_scalef32_pk_bf16_fp8 v210, v241, 1.0
	v_cvt_scalef32_pk_bf16_fp8 v211, v241, 1.0 op_sel:[1,0,0]
	v_cvt_scalef32_pk_bf16_fp8 v138, v242, 1.0
	v_cvt_scalef32_pk_bf16_fp8 v139, v242, 1.0 op_sel:[1,0,0]
	v_cvt_scalef32_pk_bf16_fp8 v140, v243, 1.0
	v_cvt_scalef32_pk_bf16_fp8 v141, v243, 1.0 op_sel:[1,0,0]
	v_mfma_f32_16x16x32_bf16 v[212:215], v[150:153], v[66:69], 0
	s_waitcnt vmcnt(5)
	v_cvt_scalef32_pk_bf16_fp8 v216, v236, 1.0
	v_cvt_scalef32_pk_bf16_fp8 v217, v236, 1.0 op_sel:[1,0,0]
	v_cvt_scalef32_pk_bf16_fp8 v218, v237, 1.0
	v_mfma_f32_16x16x32_bf16 v[220:223], v[142:145], v[82:85], 0
	v_cvt_scalef32_pk_bf16_fp8 v219, v237, 1.0 op_sel:[1,0,0]
	v_cvt_scalef32_pk_bf16_fp8 v224, v238, 1.0
	v_cvt_scalef32_pk_bf16_fp8 v225, v238, 1.0 op_sel:[1,0,0]
	v_cvt_scalef32_pk_bf16_fp8 v226, v239, 1.0
	v_cvt_scalef32_pk_bf16_fp8 v227, v239, 1.0 op_sel:[1,0,0]
	v_mfma_f32_16x16x32_bf16 v[212:215], v[208:211], v[70:73], v[212:215]
	s_waitcnt vmcnt(4)
	v_cvt_scalef32_pk_bf16_fp8 v228, v232, 1.0
	v_cvt_scalef32_pk_bf16_fp8 v229, v232, 1.0 op_sel:[1,0,0]
	v_cvt_scalef32_pk_bf16_fp8 v230, v233, 1.0
	v_mfma_f32_16x16x32_bf16 v[134:137], v[138:141], v[86:89], v[220:223]
	v_cvt_scalef32_pk_bf16_fp8 v231, v233, 1.0 op_sel:[1,0,0]
	v_max_f32_e32 v0, v149, v148
	ds_write_b128 v193, v[150:153] offset:8192
	ds_write_b128 v194, v[142:145] offset:8192
	v_cvt_scalef32_pk_bf16_fp8 v220, v234, 1.0
	v_cvt_scalef32_pk_bf16_fp8 v221, v234, 1.0 op_sel:[1,0,0]
	v_cvt_scalef32_pk_bf16_fp8 v222, v235, 1.0
	v_cvt_scalef32_pk_bf16_fp8 v223, v235, 1.0 op_sel:[1,0,0]
	global_load_dwordx4 v[244:247], v[248:249], off
	global_load_dwordx4 v[240:243], v[248:249], off offset:64
	global_load_dwordx4 v[236:239], v[248:249], off offset:128
	global_load_dwordx4 v[232:235], v[248:249], off offset:192
	v_mfma_f32_16x16x32_bf16 v[212:215], v[216:219], v[74:77], v[212:215]
	ds_write_b128 v190, v[208:211] offset:8192
	ds_write_b128 v191, v[138:141] offset:8192
	ds_write_b128 v192, v[216:219] offset:8192
	ds_write_b128 v186, v[224:227] offset:8192
	ds_write_b128 v187, v[228:231] offset:8192
	ds_write_b128 v188, v[220:223] offset:8192
	v_mfma_f32_16x16x32_bf16 v[134:137], v[224:227], v[90:93], v[134:137]
	v_mfma_f32_16x16x32_bf16 v[130:133], v[228:231], v[78:81], v[212:215]
	v_mfma_f32_16x16x32_bf16 v[134:137], v[220:223], v[94:97], v[134:137]
	s_nop 7
	v_pk_add_f32 v[132:133], v[132:133], v[136:137]
	v_pk_add_f32 v[130:131], v[130:131], v[134:135]
	v_pk_mul_f32 v[134:135], v[132:133], s[14:15] op_sel_hi:[1,0]
	v_pk_mul_f32 v[130:131], v[130:131], s[14:15] op_sel_hi:[1,0]
	s_waitcnt lgkmcnt(11)
	v_add_f32_e32 v133, v204, v130
	s_waitcnt lgkmcnt(10)
	v_add_f32_e32 v132, v205, v131
	s_waitcnt lgkmcnt(9)
	v_add_f32_e32 v131, v206, v134
	s_waitcnt lgkmcnt(8)
	v_add_f32_e32 v130, v207, v135
	v_max_f32_e32 v135, v131, v130
	v_max_f32_e32 v134, v147, v146
	v_max3_f32 v135, v133, v132, v135
	v_max3_f32 v0, v0, v134, v135
	v_mov_b32_e32 v134, v0
	s_nop 1
	v_permlane16_swap_b32_e32 v0, v134
	v_max_f32_e32 v134, v134, v134
	v_max_f32_e32 v0, v0, v0
	v_max_f32_e32 v0, v0, v134
	v_mov_b32_e32 v134, v0
	s_nop 1
	v_permlane32_swap_b32_e32 v0, v134
	v_max_f32_e32 v134, v134, v134
	v_max_f32_e32 v0, v0, v0
	v_max_f32_e32 v0, v0, v134
	v_add_f32_e32 v134, 0x41000000, v200
	v_cmp_gt_f32_e32 vcc, v0, v134
	s_nop 1
	v_cndmask_b32_e32 v0, v200, v0, vcc
	v_sub_f32_e32 v134, v200, v0
	v_exp_f32_e32 v134, v134
	s_nop 0
	v_cmp_neq_f32_e32 vcc, 1.0, v134
	s_cbranch_vccz .LBB0_1467
	ds_bpermute_b32 v136, v167, v134
	ds_bpermute_b32 v138, v165, v134
	ds_bpermute_b32 v139, v166, v134
	ds_bpermute_b32 v137, v168, v134
	s_waitcnt lgkmcnt(1)
	v_pk_mul_f32 v[64:65], v[64:65], v[138:139]
	s_waitcnt lgkmcnt(0)
	v_pk_mul_f32 v[62:63], v[62:63], v[136:137]
	v_pk_mul_f32 v[60:61], v[60:61], v[138:139]
	v_pk_mul_f32 v[58:59], v[58:59], v[136:137]
	v_pk_mul_f32 v[56:57], v[56:57], v[138:139]
	v_pk_mul_f32 v[54:55], v[54:55], v[136:137]
	v_pk_mul_f32 v[52:53], v[52:53], v[138:139]
	v_pk_mul_f32 v[50:51], v[50:51], v[136:137]
	v_pk_mul_f32 v[48:49], v[48:49], v[138:139]
	v_pk_mul_f32 v[46:47], v[46:47], v[136:137]
	v_pk_mul_f32 v[44:45], v[44:45], v[138:139]
	v_pk_mul_f32 v[42:43], v[42:43], v[136:137]
	v_pk_mul_f32 v[40:41], v[40:41], v[138:139]
	v_pk_mul_f32 v[38:39], v[38:39], v[136:137]
	v_pk_mul_f32 v[36:37], v[36:37], v[138:139]
	v_pk_mul_f32 v[34:35], v[34:35], v[136:137]
	v_pk_mul_f32 v[32:33], v[32:33], v[138:139]
	v_pk_mul_f32 v[30:31], v[30:31], v[136:137]
	v_pk_mul_f32 v[28:29], v[28:29], v[138:139]
	v_pk_mul_f32 v[26:27], v[26:27], v[136:137]
	v_pk_mul_f32 v[24:25], v[24:25], v[138:139]
	v_pk_mul_f32 v[22:23], v[22:23], v[136:137]
	v_pk_mul_f32 v[20:21], v[20:21], v[138:139]
	v_pk_mul_f32 v[18:19], v[18:19], v[136:137]
	v_pk_mul_f32 v[16:17], v[16:17], v[138:139]
	v_pk_mul_f32 v[14:15], v[14:15], v[136:137]
	v_pk_mul_f32 v[12:13], v[12:13], v[138:139]
	v_pk_mul_f32 v[10:11], v[10:11], v[136:137]
	v_pk_mul_f32 v[8:9], v[8:9], v[138:139]
	v_pk_mul_f32 v[6:7], v[6:7], v[136:137]
	v_pk_mul_f32 v[4:5], v[4:5], v[138:139]
	v_pk_mul_f32 v[2:3], v[2:3], v[136:137]
.LBB0_1467:
	v_sub_f32_e32 v131, v131, v0
	v_sub_f32_e32 v135, v149, v0
	v_sub_f32_e32 v136, v148, v0
	v_sub_f32_e32 v137, v147, v0
	v_exp_f32_e32 v138, v131
	v_sub_f32_e32 v131, v146, v0
	v_exp_f32_e32 v135, v135
	v_exp_f32_e32 v136, v136
	v_exp_f32_e32 v137, v137
	v_exp_f32_e32 v131, v131
	v_sub_f32_e32 v133, v133, v0
	v_sub_f32_e32 v132, v132, v0
	v_sub_f32_e32 v130, v130, v0
	v_exp_f32_e32 v133, v133
	v_exp_f32_e32 v132, v132
	v_exp_f32_e32 v139, v130
	v_add_f32_e32 v130, v135, v136
	v_add_f32_e32 v140, v137, v131
	v_add_f32_e32 v130, v130, v140
	v_fmac_f32_e32 v130, v185, v134
	v_add_f32_e32 v134, v133, v132
	v_add_f32_e32 v140, v138, v139
	v_add_f32_e32 v134, v134, v140
	v_add_f32_e32 v185, v134, v130
	v_cvt_pk_bf16_f32 v130, v135, v136
	ds_read_b64_tr_b16 v[134:135],v177
	v_cvt_pk_bf16_f32 v131, v137, v131
	ds_read_b64_tr_b16 v[136:137],v177 offset:8192
	v_cvt_pk_bf16_f32 v132, v133, v132
	v_cvt_pk_bf16_f32 v133, v138, v139
	ds_read_b64_tr_b16 v[138:139],v178
	ds_read_b64_tr_b16 v[140:141],v178 offset:8192
	ds_read_b64_tr_b16 v[142:143],v179
	ds_read_b64_tr_b16 v[144:145],v179 offset:8192
	ds_read_b64_tr_b16 v[146:147],v180
	ds_read_b64_tr_b16 v[148:149],v180 offset:8192
	ds_read_b64_tr_b16 v[150:151],v181
	ds_read_b64_tr_b16 v[152:153],v181 offset:8192
	ds_read_b64_tr_b16 v[200:201],v182
	ds_read_b64_tr_b16 v[202:203],v182 offset:8192
	ds_read_b64_tr_b16 v[204:205],v183
	ds_read_b64_tr_b16 v[206:207],v183 offset:8192
	ds_read_b64_tr_b16 v[208:209],v184
	ds_read_b64_tr_b16 v[210:211],v184 offset:8192
	s_waitcnt lgkmcnt(0)
	s_nop 1
	v_mfma_f32_16x16x32_bf16 v[62:65], v[130:133], v[134:137], v[62:65]
	ds_read_b64_tr_b16 v[134:135],v175
	ds_read_b64_tr_b16 v[136:137],v175 offset:8192
	v_mfma_f32_16x16x32_bf16 v[58:61], v[130:133], v[138:141], v[58:61]
	ds_read_b64_tr_b16 v[138:139],v176
	ds_read_b64_tr_b16 v[140:141],v176 offset:8192
	v_mfma_f32_16x16x32_bf16 v[54:57], v[130:133], v[142:145], v[54:57]
	ds_read_b64_tr_b16 v[142:143],v174
	ds_read_b64_tr_b16 v[144:145],v174 offset:8192
	v_mfma_f32_16x16x32_bf16 v[50:53], v[130:133], v[146:149], v[50:53]
	ds_read_b64_tr_b16 v[146:147],v172
	ds_read_b64_tr_b16 v[148:149],v172 offset:8192
	v_mfma_f32_16x16x32_bf16 v[46:49], v[130:133], v[150:153], v[46:49]
	ds_read_b64_tr_b16 v[150:151],v173
	ds_read_b64_tr_b16 v[152:153],v173 offset:8192
	v_mfma_f32_16x16x32_bf16 v[42:45], v[130:133], v[200:203], v[42:45]
	ds_read_b64_tr_b16 v[200:201],v171
	ds_read_b64_tr_b16 v[202:203],v171 offset:8192
	ds_read_b64_tr_b16 v[212:213],v169
	ds_read_b64_tr_b16 v[214:215],v169 offset:8192
	v_mfma_f32_16x16x32_bf16 v[38:41], v[130:133], v[204:207], v[38:41]
	ds_read_b64_tr_b16 v[204:205],v170
	ds_read_b64_tr_b16 v[206:207],v170 offset:8192
	s_waitcnt lgkmcnt(0)
	v_mfma_f32_16x16x32_bf16 v[34:37], v[130:133], v[208:211], v[34:37]
	v_mfma_f32_16x16x32_bf16 v[30:33], v[130:133], v[134:137], v[30:33]
	s_add_i32 s17, s17, 2
	v_add_u32_e32 v198, 32, v198
	v_add_u32_e32 v199, 32, v199
	v_mfma_f32_16x16x32_bf16 v[26:29], v[130:133], v[138:141], v[26:29]
	s_and_b64 vcc, exec, s[20:21]
	v_mfma_f32_16x16x32_bf16 v[22:25], v[130:133], v[142:145], v[22:25]
	v_mfma_f32_16x16x32_bf16 v[18:21], v[130:133], v[146:149], v[18:21]
	v_mfma_f32_16x16x32_bf16 v[14:17], v[130:133], v[150:153], v[14:17]
	v_mfma_f32_16x16x32_bf16 v[10:13], v[130:133], v[200:203], v[10:13]
	v_mfma_f32_16x16x32_bf16 v[6:9], v[130:133], v[212:215], v[6:9]
	v_mfma_f32_16x16x32_bf16 v[2:5], v[130:133], v[204:207], v[2:5]
	s_cbranch_vccnz .LBB0_1469
	v_mov_b32_e32 v200, v0
	s_branch .LBB0_1463
.LBB0_1469:
	v_lshlrev_b32_e32 v130, 6, v197
	v_and_b32_e32 v130, 0x3fc0, v130
	v_bfe_u32 v131, v197, 8, 8
	v_bfe_u32 v132, v197, 16, 8
	v_lshrrev_b32_e32 v133, 24, v197
	v_add_u32_e32 v130, v189, v130
	v_lshl_add_u32 v131, v131, 6, v189
	v_lshl_add_u32 v132, v132, 6, v189
	v_lshl_add_u32 v133, v133, 6, v189
	ds_read_b32 v156, v195 offset:240
	ds_read_b32 v157, v130
	ds_read_b32 v195, v131
	ds_read_b32 v196, v132
	ds_read_b32 v197, v133
	s_waitcnt vmcnt(4)
	v_cvt_scalef32_pk_bf16_fp8 v142, v98, 1.0
	v_cvt_scalef32_pk_bf16_fp8 v143, v98, 1.0 op_sel:[1,0,0]
	v_cvt_scalef32_pk_bf16_fp8 v144, v99, 1.0
	v_cvt_scalef32_pk_bf16_fp8 v145, v99, 1.0 op_sel:[1,0,0]
	v_cvt_scalef32_pk_bf16_fp8 v98, v100, 1.0
	v_cvt_scalef32_pk_bf16_fp8 v99, v100, 1.0 op_sel:[1,0,0]
	v_cvt_scalef32_pk_bf16_fp8 v100, v101, 1.0
	v_cvt_scalef32_pk_bf16_fp8 v101, v101, 1.0 op_sel:[1,0,0]
	v_cvt_scalef32_pk_bf16_fp8 v130, v110, 1.0
	v_cvt_scalef32_pk_bf16_fp8 v131, v110, 1.0 op_sel:[1,0,0]
	v_cvt_scalef32_pk_bf16_fp8 v132, v111, 1.0
	v_cvt_scalef32_pk_bf16_fp8 v133, v111, 1.0 op_sel:[1,0,0]
	v_cvt_scalef32_pk_bf16_fp8 v110, v112, 1.0
	v_cvt_scalef32_pk_bf16_fp8 v111, v112, 1.0 op_sel:[1,0,0]
	v_cvt_scalef32_pk_bf16_fp8 v112, v113, 1.0
	v_cvt_scalef32_pk_bf16_fp8 v113, v113, 1.0 op_sel:[1,0,0]
	v_cvt_scalef32_pk_bf16_fp8 v134, v106, 1.0
	v_cvt_scalef32_pk_bf16_fp8 v135, v106, 1.0 op_sel:[1,0,0]
	v_cvt_scalef32_pk_bf16_fp8 v136, v107, 1.0
	v_cvt_scalef32_pk_bf16_fp8 v137, v107, 1.0 op_sel:[1,0,0]
	v_cvt_scalef32_pk_bf16_fp8 v106, v108, 1.0
	v_cvt_scalef32_pk_bf16_fp8 v107, v108, 1.0 op_sel:[1,0,0]
	v_cvt_scalef32_pk_bf16_fp8 v108, v109, 1.0
	v_cvt_scalef32_pk_bf16_fp8 v109, v109, 1.0 op_sel:[1,0,0]
	v_cvt_scalef32_pk_bf16_fp8 v138, v102, 1.0
	v_cvt_scalef32_pk_bf16_fp8 v139, v102, 1.0 op_sel:[1,0,0]
	v_cvt_scalef32_pk_bf16_fp8 v140, v103, 1.0
	v_cvt_scalef32_pk_bf16_fp8 v141, v103, 1.0 op_sel:[1,0,0]
	v_cvt_scalef32_pk_bf16_fp8 v102, v104, 1.0
	v_cvt_scalef32_pk_bf16_fp8 v103, v104, 1.0 op_sel:[1,0,0]
	v_cvt_scalef32_pk_bf16_fp8 v104, v105, 1.0
	v_cvt_scalef32_pk_bf16_fp8 v105, v105, 1.0 op_sel:[1,0,0]
	v_mfma_f32_16x16x32_bf16 v[146:149], v[130:133], v[66:69], 0
	ds_write_b128 v193, v[130:133]
	ds_write_b128 v194, v[110:113]
	ds_write_b128 v190, v[134:137]
	ds_write_b128 v191, v[106:109]
	ds_write_b128 v192, v[138:141]
	ds_write_b128 v186, v[102:105]
	ds_write_b128 v187, v[142:145]
	ds_write_b128 v188, v[98:101]
	v_mfma_f32_16x16x32_bf16 v[150:153], v[110:113], v[82:85], 0
	v_mfma_f32_16x16x32_bf16 v[146:149], v[134:137], v[70:73], v[146:149]
	v_mfma_f32_16x16x32_bf16 v[150:153], v[106:109], v[86:89], v[150:153]
	v_mfma_f32_16x16x32_bf16 v[146:149], v[138:141], v[74:77], v[146:149]
	v_mfma_f32_16x16x32_bf16 v[110:113], v[102:105], v[90:93], v[150:153]
	s_waitcnt lgkmcnt(12)
	v_bfe_u32 v104, v156, 16, 8
	v_lshrrev_b32_e32 v105, 24, v156
	v_lshl_add_u32 v104, v104, 6, v189
	v_mfma_f32_16x16x32_bf16 v[106:109], v[142:145], v[78:81], v[146:149]
	v_lshl_add_u32 v105, v105, 6, v189
	v_mfma_f32_16x16x32_bf16 v[98:101], v[98:101], v[94:97], v[110:113]
	s_nop 7
	v_pk_add_f32 v[100:101], v[108:109], v[100:101]
	v_pk_add_f32 v[98:99], v[106:107], v[98:99]
	v_pk_mul_f32 v[102:103], v[100:101], s[14:15] op_sel_hi:[1,0]
	v_lshlrev_b32_e32 v100, 6, v156
	v_and_b32_e32 v100, 0x3fc0, v100
	v_add_u32_e32 v100, v189, v100
	v_bfe_u32 v101, v156, 8, 8
	v_lshl_add_u32 v101, v101, 6, v189
	ds_read_b32 v134, v100
	ds_read_b32 v135, v101
	ds_read_b32 v136, v104
	ds_read_b32 v137, v105
	v_pk_mul_f32 v[98:99], v[98:99], s[14:15] op_sel_hi:[1,0]
	s_waitcnt lgkmcnt(14)
	v_add_f32_e32 v101, v157, v98
	v_add_f32_e32 v100, v195, v99
	s_waitcnt lgkmcnt(13)
	v_add_f32_e32 v99, v196, v102
	s_waitcnt lgkmcnt(12)
	v_add_f32_e32 v98, v197, v103
	s_waitcnt vmcnt(3)
	v_cvt_scalef32_pk_bf16_fp8 v102, v244, 1.0
	v_cvt_scalef32_pk_bf16_fp8 v103, v244, 1.0 op_sel:[1,0,0]
	v_cvt_scalef32_pk_bf16_fp8 v104, v245, 1.0
	v_cvt_scalef32_pk_bf16_fp8 v105, v245, 1.0 op_sel:[1,0,0]
	v_cvt_scalef32_pk_bf16_fp8 v106, v246, 1.0
	v_cvt_scalef32_pk_bf16_fp8 v107, v246, 1.0 op_sel:[1,0,0]
	v_cvt_scalef32_pk_bf16_fp8 v108, v247, 1.0
	v_cvt_scalef32_pk_bf16_fp8 v109, v247, 1.0 op_sel:[1,0,0]
	s_waitcnt vmcnt(2)
	v_cvt_scalef32_pk_bf16_fp8 v110, v240, 1.0
	v_cvt_scalef32_pk_bf16_fp8 v111, v240, 1.0 op_sel:[1,0,0]
	v_cvt_scalef32_pk_bf16_fp8 v112, v241, 1.0
	v_cvt_scalef32_pk_bf16_fp8 v113, v241, 1.0 op_sel:[1,0,0]
	v_cvt_scalef32_pk_bf16_fp8 v122, v242, 1.0
	v_cvt_scalef32_pk_bf16_fp8 v123, v242, 1.0 op_sel:[1,0,0]
	v_cvt_scalef32_pk_bf16_fp8 v124, v243, 1.0
	v_cvt_scalef32_pk_bf16_fp8 v125, v243, 1.0 op_sel:[1,0,0]
	s_waitcnt vmcnt(1)
	v_cvt_scalef32_pk_bf16_fp8 v126, v236, 1.0
	v_cvt_scalef32_pk_bf16_fp8 v127, v236, 1.0 op_sel:[1,0,0]
	v_cvt_scalef32_pk_bf16_fp8 v128, v237, 1.0
	v_cvt_scalef32_pk_bf16_fp8 v129, v237, 1.0 op_sel:[1,0,0]
	v_cvt_scalef32_pk_bf16_fp8 v118, v238, 1.0
	v_cvt_scalef32_pk_bf16_fp8 v119, v238, 1.0 op_sel:[1,0,0]
	v_cvt_scalef32_pk_bf16_fp8 v120, v239, 1.0
	v_cvt_scalef32_pk_bf16_fp8 v121, v239, 1.0 op_sel:[1,0,0]
	s_waitcnt vmcnt(0)
	v_cvt_scalef32_pk_bf16_fp8 v130, v232, 1.0
	v_cvt_scalef32_pk_bf16_fp8 v131, v232, 1.0 op_sel:[1,0,0]
	v_cvt_scalef32_pk_bf16_fp8 v132, v233, 1.0
	v_cvt_scalef32_pk_bf16_fp8 v133, v233, 1.0 op_sel:[1,0,0]
	v_cvt_scalef32_pk_bf16_fp8 v114, v234, 1.0
	v_cvt_scalef32_pk_bf16_fp8 v115, v234, 1.0 op_sel:[1,0,0]
	v_cvt_scalef32_pk_bf16_fp8 v116, v235, 1.0
	v_cvt_scalef32_pk_bf16_fp8 v117, v235, 1.0 op_sel:[1,0,0]
	v_mfma_f32_16x16x32_bf16 v[82:85], v[106:109], v[82:85], 0
	ds_write_b128 v193, v[102:105] offset:8192
	ds_write_b128 v194, v[106:109] offset:8192
	ds_write_b128 v190, v[110:113] offset:8192
	ds_write_b128 v191, v[122:125] offset:8192
	ds_write_b128 v192, v[126:129] offset:8192
	ds_write_b128 v186, v[118:121] offset:8192
	ds_write_b128 v187, v[130:133] offset:8192
	ds_write_b128 v188, v[114:117] offset:8192
	v_mfma_f32_16x16x32_bf16 v[66:69], v[102:105], v[66:69], 0
	v_mfma_f32_16x16x32_bf16 v[82:85], v[122:125], v[86:89], v[82:85]
	v_mfma_f32_16x16x32_bf16 v[66:69], v[110:113], v[70:73], v[66:69]
	v_mfma_f32_16x16x32_bf16 v[82:85], v[118:121], v[90:93], v[82:85]
	v_mfma_f32_16x16x32_bf16 v[66:69], v[126:129], v[74:77], v[66:69]
	v_mfma_f32_16x16x32_bf16 v[82:85], v[114:117], v[94:97], v[82:85]
	v_mfma_f32_16x16x32_bf16 v[66:69], v[130:133], v[78:81], v[66:69]
	s_nop 7
	v_pk_add_f32 v[68:69], v[84:85], v[68:69]
	v_pk_add_f32 v[66:67], v[82:83], v[66:67]
	v_pk_mul_f32 v[70:71], v[68:69], s[14:15] op_sel_hi:[1,0]
	v_pk_mul_f32 v[66:67], v[66:67], s[14:15] op_sel_hi:[1,0]
	s_waitcnt lgkmcnt(11)
	v_add_f32_e32 v69, v134, v66
	s_waitcnt lgkmcnt(10)
	v_add_f32_e32 v68, v135, v67
	s_waitcnt lgkmcnt(9)
	v_add_f32_e32 v67, v136, v70
	s_waitcnt lgkmcnt(8)
	v_add_f32_e32 v66, v137, v71
	v_max_f32_e32 v72, v67, v66
	v_max_f32_e32 v70, v101, v100
	v_max_f32_e32 v71, v99, v98
	v_max3_f32 v72, v69, v68, v72
	v_max3_f32 v70, v70, v71, v72
	v_mov_b32_e32 v71, v70
	s_nop 1
	v_permlane16_swap_b32_e32 v70, v71
	v_max_f32_e32 v71, v71, v71
	v_max_f32_e32 v70, v70, v70
	v_max_f32_e32 v70, v70, v71
	v_mov_b32_e32 v71, v70
	s_nop 1
	v_permlane32_swap_b32_e32 v70, v71
	v_max_f32_e32 v71, v71, v71
	v_max_f32_e32 v70, v70, v70
	v_max_f32_e32 v70, v70, v71
	v_add_f32_e32 v71, 0x41000000, v0
	v_cmp_gt_f32_e32 vcc, v70, v71
	s_nop 1
	v_cndmask_b32_e32 v70, v0, v70, vcc
	v_sub_f32_e32 v0, v0, v70
	v_exp_f32_e32 v0, v0
	s_nop 0
	v_cmp_neq_f32_e32 vcc, 1.0, v0
	s_cbranch_vccz .LBB0_1471
	ds_bpermute_b32 v72, v167, v0
	ds_bpermute_b32 v74, v165, v0
	ds_bpermute_b32 v75, v166, v0
	ds_bpermute_b32 v73, v168, v0
	s_waitcnt lgkmcnt(1)
	v_pk_mul_f32 v[64:65], v[64:65], v[74:75]
	s_waitcnt lgkmcnt(0)
	v_pk_mul_f32 v[62:63], v[62:63], v[72:73]
	v_pk_mul_f32 v[60:61], v[60:61], v[74:75]
	v_pk_mul_f32 v[58:59], v[58:59], v[72:73]
	v_pk_mul_f32 v[56:57], v[56:57], v[74:75]
	v_pk_mul_f32 v[54:55], v[54:55], v[72:73]
	v_pk_mul_f32 v[52:53], v[52:53], v[74:75]
	v_pk_mul_f32 v[50:51], v[50:51], v[72:73]
	v_pk_mul_f32 v[48:49], v[48:49], v[74:75]
	v_pk_mul_f32 v[46:47], v[46:47], v[72:73]
	v_pk_mul_f32 v[44:45], v[44:45], v[74:75]
	v_pk_mul_f32 v[42:43], v[42:43], v[72:73]
	v_pk_mul_f32 v[40:41], v[40:41], v[74:75]
	v_pk_mul_f32 v[38:39], v[38:39], v[72:73]
	v_pk_mul_f32 v[36:37], v[36:37], v[74:75]
	v_pk_mul_f32 v[34:35], v[34:35], v[72:73]
	v_pk_mul_f32 v[32:33], v[32:33], v[74:75]
	v_pk_mul_f32 v[30:31], v[30:31], v[72:73]
	v_pk_mul_f32 v[28:29], v[28:29], v[74:75]
	v_pk_mul_f32 v[26:27], v[26:27], v[72:73]
	v_pk_mul_f32 v[24:25], v[24:25], v[74:75]
	v_pk_mul_f32 v[22:23], v[22:23], v[72:73]
	v_pk_mul_f32 v[20:21], v[20:21], v[74:75]
	v_pk_mul_f32 v[18:19], v[18:19], v[72:73]
	v_pk_mul_f32 v[16:17], v[16:17], v[74:75]
	v_pk_mul_f32 v[14:15], v[14:15], v[72:73]
	v_pk_mul_f32 v[12:13], v[12:13], v[74:75]
	v_pk_mul_f32 v[10:11], v[10:11], v[72:73]
	v_pk_mul_f32 v[8:9], v[8:9], v[74:75]
	v_pk_mul_f32 v[6:7], v[6:7], v[72:73]
	v_pk_mul_f32 v[4:5], v[4:5], v[74:75]
	v_pk_mul_f32 v[2:3], v[2:3], v[72:73]
